# P9 expert-down epilogue staged through LDS so each global store writes full 128B lines (8 dwordx4 stores per wave instead of 16 partial-line dwordx2)
# speedup vs baseline: 1.0197x; 1.0104x over previous
.LBB0_996:
	s_lshl_b32 s21, s23, 10
	s_and_b32 s21, s21, 0x400
	s_nop 15
	s_nop 15
	v_add_u32_e32 v2, s21, v205
	ds_read_b128 v[12:15], v2
	ds_read_b128 v[16:19], v2 offset:16
	ds_read_b128 v[4:7], v2 offset:512
	ds_read_b128 v[8:11], v2 offset:528
	v_and_b32_e32 v36, 15, v221
	v_lshrrev_b32_e32 v37, 2, v221
	v_and_b32_e32 v37, 16, v37
	v_or_b32_e32 v37, v37, v36
	v_lshrrev_b32_e32 v38, 4, v209
	v_xor_b32_e32 v38, v38, v36
	v_lshlrev_b32_e32 v38, 4, v38
	v_and_b32_e32 v39, 8, v209
	v_or_b32_e32 v38, v38, v39
	v_lshl_or_b32 v40, v37, 8, v38
	v_add_u32_e32 v40, 0x21800, v40
	v_xor_b32_e32 v41, 0x80, v40
	v_lshrrev_b32_e32 v42, 4, v0
	v_and_b32_e32 v43, 15, v0
	v_xor_b32_e32 v44, v43, v42
	v_and_b32_e32 v44, 15, v44
	v_lshlrev_b32_e32 v44, 4, v44
	v_lshl_or_b32 v47, v42, 8, v44
	v_add_u32_e32 v47, 0x21800, v47
	v_and_b32_e32 v45, 15, v42
	v_lshrrev_b32_e32 v46, 4, v42
	v_lshl_or_b32 v45, v46, 6, v45
	v_lshlrev_b32_e32 v45, 10, v45
	v_lshl_or_b32 v45, v43, 4, v45
	s_lshl_b32 s3, s22, 8
	s_and_b32 s3, s3, 0x300
	s_lshl_b32 s40, s69, 18
	s_add_i32 s3, s3, s40
	s_add_u32 s40, s14, s3
	s_addc_u32 s41, s15, 0
	s_waitcnt lgkmcnt(0)
	v_pk_add_f32 v[20:21], v[80:81], v[12:13]
	v_pk_add_f32 v[22:23], v[88:89], v[16:17]
	v_mov_b32_e32 v28, v3
	v_mov_b32_e32 v29, v3
	v_pk_add_f32 v[24:25], v[82:83], v[14:15]
	v_pk_add_f32 v[26:27], v[90:91], v[18:19]
	v_cvt_pk_fp8_f32 v28, v20, v21
	v_cvt_pk_fp8_f32 v29, v22, v23
	v_cvt_pk_fp8_f32 v28, v24, v25 op_sel:[0,0,1]
	v_cvt_pk_fp8_f32 v29, v26, v27 op_sel:[0,0,1]
	v_pk_add_f32 v[20:21], v[144:145], v[4:5]
	v_pk_add_f32 v[22:23], v[154:155], v[8:9]
	v_mov_b32_e32 v30, v3
	v_mov_b32_e32 v31, v3
	v_pk_add_f32 v[24:25], v[146:147], v[6:7]
	v_pk_add_f32 v[26:27], v[156:157], v[10:11]
	v_cvt_pk_fp8_f32 v30, v20, v21
	v_cvt_pk_fp8_f32 v31, v22, v23
	v_cvt_pk_fp8_f32 v30, v24, v25 op_sel:[0,0,1]
	v_cvt_pk_fp8_f32 v31, v26, v27 op_sel:[0,0,1]
	ds_write_b64 v40, v[28:29]
	ds_write_b64 v41, v[30:31]
	v_pk_add_f32 v[20:21], v[96:97], v[12:13]
	v_pk_add_f32 v[22:23], v[104:105], v[16:17]
	v_mov_b32_e32 v56, v3
	v_mov_b32_e32 v57, v3
	v_pk_add_f32 v[24:25], v[98:99], v[14:15]
	v_pk_add_f32 v[26:27], v[106:107], v[18:19]
	v_cvt_pk_fp8_f32 v56, v20, v21
	v_cvt_pk_fp8_f32 v57, v22, v23
	v_cvt_pk_fp8_f32 v56, v24, v25 op_sel:[0,0,1]
	v_cvt_pk_fp8_f32 v57, v26, v27 op_sel:[0,0,1]
	v_pk_add_f32 v[20:21], v[158:159], v[4:5]
	v_pk_add_f32 v[22:23], v[162:163], v[8:9]
	v_mov_b32_e32 v58, v3
	v_mov_b32_e32 v59, v3
	v_pk_add_f32 v[24:25], v[160:161], v[6:7]
	v_pk_add_f32 v[26:27], v[164:165], v[10:11]
	v_cvt_pk_fp8_f32 v58, v20, v21
	v_cvt_pk_fp8_f32 v59, v22, v23
	v_cvt_pk_fp8_f32 v58, v24, v25 op_sel:[0,0,1]
	v_cvt_pk_fp8_f32 v59, v26, v27 op_sel:[0,0,1]
	s_waitcnt lgkmcnt(0)
	s_barrier
	ds_read_b128 v[32:35], v47
	ds_write_b64 v40, v[56:57] offset:12288
	ds_write_b64 v41, v[58:59] offset:12288
	s_waitcnt lgkmcnt(2)
	global_store_dwordx4 v45, v[32:35], s[40:41]
	s_add_u32 s40, s40, 0x4000
	s_addc_u32 s41, s41, 0
	v_pk_add_f32 v[20:21], v[112:113], v[12:13]
	v_pk_add_f32 v[22:23], v[120:121], v[16:17]
	v_mov_b32_e32 v28, v3
	v_mov_b32_e32 v29, v3
	v_pk_add_f32 v[24:25], v[114:115], v[14:15]
	v_pk_add_f32 v[26:27], v[122:123], v[18:19]
	v_cvt_pk_fp8_f32 v28, v20, v21
	v_cvt_pk_fp8_f32 v29, v22, v23
	v_cvt_pk_fp8_f32 v28, v24, v25 op_sel:[0,0,1]
	v_cvt_pk_fp8_f32 v29, v26, v27 op_sel:[0,0,1]
	v_pk_add_f32 v[20:21], v[166:167], v[4:5]
	v_pk_add_f32 v[22:23], v[170:171], v[8:9]
	v_mov_b32_e32 v30, v3
	v_mov_b32_e32 v31, v3
	v_pk_add_f32 v[24:25], v[168:169], v[6:7]
	v_pk_add_f32 v[26:27], v[172:173], v[10:11]
	v_cvt_pk_fp8_f32 v30, v20, v21
	v_cvt_pk_fp8_f32 v31, v22, v23
	v_cvt_pk_fp8_f32 v30, v24, v25 op_sel:[0,0,1]
	v_cvt_pk_fp8_f32 v31, v26, v27 op_sel:[0,0,1]
	s_waitcnt lgkmcnt(0)
	s_barrier
	ds_read_b128 v[48:51], v47 offset:12288
	ds_write_b64 v40, v[28:29]
	ds_write_b64 v41, v[30:31]
	s_waitcnt lgkmcnt(2)
	global_store_dwordx4 v45, v[48:51], s[40:41]
	s_add_u32 s40, s40, 0x4000
	s_addc_u32 s41, s41, 0
	v_pk_add_f32 v[20:21], v[128:129], v[12:13]
	v_pk_add_f32 v[22:23], v[132:133], v[16:17]
	v_mov_b32_e32 v56, v3
	v_mov_b32_e32 v57, v3
	v_pk_add_f32 v[24:25], v[130:131], v[14:15]
	v_pk_add_f32 v[26:27], v[134:135], v[18:19]
	v_cvt_pk_fp8_f32 v56, v20, v21
	v_cvt_pk_fp8_f32 v57, v22, v23
	v_cvt_pk_fp8_f32 v56, v24, v25 op_sel:[0,0,1]
	v_cvt_pk_fp8_f32 v57, v26, v27 op_sel:[0,0,1]
	v_pk_add_f32 v[20:21], v[174:175], v[4:5]
	v_pk_add_f32 v[22:23], v[182:183], v[8:9]
	v_mov_b32_e32 v58, v3
	v_mov_b32_e32 v59, v3
	v_pk_add_f32 v[24:25], v[176:177], v[6:7]
	v_pk_add_f32 v[26:27], v[184:185], v[10:11]
	v_cvt_pk_fp8_f32 v58, v20, v21
	v_cvt_pk_fp8_f32 v59, v22, v23
	v_cvt_pk_fp8_f32 v58, v24, v25 op_sel:[0,0,1]
	v_cvt_pk_fp8_f32 v59, v26, v27 op_sel:[0,0,1]
	s_waitcnt lgkmcnt(0)
	s_barrier
	ds_read_b128 v[32:35], v47
	ds_write_b64 v40, v[56:57] offset:12288
	ds_write_b64 v41, v[58:59] offset:12288
	s_waitcnt lgkmcnt(2)
	global_store_dwordx4 v45, v[32:35], s[40:41]
	s_add_u32 s40, s40, 0x4000
	s_addc_u32 s41, s41, 0
	v_pk_add_f32 v[20:21], v[68:69], v[12:13]
	v_pk_add_f32 v[22:23], v[72:73], v[16:17]
	v_mov_b32_e32 v28, v3
	v_mov_b32_e32 v29, v3
	v_pk_add_f32 v[24:25], v[70:71], v[14:15]
	v_pk_add_f32 v[26:27], v[74:75], v[18:19]
	v_cvt_pk_fp8_f32 v28, v20, v21
	v_cvt_pk_fp8_f32 v29, v22, v23
	v_cvt_pk_fp8_f32 v28, v24, v25 op_sel:[0,0,1]
	v_cvt_pk_fp8_f32 v29, v26, v27 op_sel:[0,0,1]
	v_pk_add_f32 v[20:21], v[124:125], v[4:5]
	v_pk_add_f32 v[22:23], v[136:137], v[8:9]
	v_mov_b32_e32 v30, v3
	v_mov_b32_e32 v31, v3
	v_pk_add_f32 v[24:25], v[126:127], v[6:7]
	v_pk_add_f32 v[26:27], v[138:139], v[10:11]
	v_cvt_pk_fp8_f32 v30, v20, v21
	v_cvt_pk_fp8_f32 v31, v22, v23
	v_cvt_pk_fp8_f32 v30, v24, v25 op_sel:[0,0,1]
	v_cvt_pk_fp8_f32 v31, v26, v27 op_sel:[0,0,1]
	s_waitcnt lgkmcnt(0)
	s_barrier
	ds_read_b128 v[48:51], v47 offset:12288
	ds_write_b64 v40, v[28:29]
	ds_write_b64 v41, v[30:31]
	s_waitcnt lgkmcnt(2)
	global_store_dwordx4 v45, v[48:51], s[40:41]
	s_add_u32 s40, s40, 0x14000
	s_addc_u32 s41, s41, 0
	v_pk_add_f32 v[20:21], v[76:77], v[12:13]
	v_pk_add_f32 v[22:23], v[84:85], v[16:17]
	v_mov_b32_e32 v56, v3
	v_mov_b32_e32 v57, v3
	v_pk_add_f32 v[24:25], v[78:79], v[14:15]
	v_pk_add_f32 v[26:27], v[86:87], v[18:19]
	v_cvt_pk_fp8_f32 v56, v20, v21
	v_cvt_pk_fp8_f32 v57, v22, v23
	v_cvt_pk_fp8_f32 v56, v24, v25 op_sel:[0,0,1]
	v_cvt_pk_fp8_f32 v57, v26, v27 op_sel:[0,0,1]
	v_pk_add_f32 v[20:21], v[140:141], v[4:5]
	v_pk_add_f32 v[22:23], v[150:151], v[8:9]
	v_mov_b32_e32 v58, v3
	v_mov_b32_e32 v59, v3
	v_pk_add_f32 v[24:25], v[142:143], v[6:7]
	v_pk_add_f32 v[26:27], v[152:153], v[10:11]
	v_cvt_pk_fp8_f32 v58, v20, v21
	v_cvt_pk_fp8_f32 v59, v22, v23
	v_cvt_pk_fp8_f32 v58, v24, v25 op_sel:[0,0,1]
	v_cvt_pk_fp8_f32 v59, v26, v27 op_sel:[0,0,1]
	s_waitcnt lgkmcnt(0)
	s_barrier
	ds_read_b128 v[32:35], v47
	ds_write_b64 v40, v[56:57] offset:12288
	ds_write_b64 v41, v[58:59] offset:12288
	s_waitcnt lgkmcnt(2)
	global_store_dwordx4 v45, v[32:35], s[40:41]
	s_add_u32 s40, s40, 0x4000
	s_addc_u32 s41, s41, 0
	v_pk_add_f32 v[20:21], v[92:93], v[12:13]
	v_pk_add_f32 v[22:23], v[100:101], v[16:17]
	v_mov_b32_e32 v28, v3
	v_mov_b32_e32 v29, v3
	v_pk_add_f32 v[24:25], v[94:95], v[14:15]
	v_pk_add_f32 v[26:27], v[102:103], v[18:19]
	v_cvt_pk_fp8_f32 v28, v20, v21
	v_cvt_pk_fp8_f32 v29, v22, v23
	v_cvt_pk_fp8_f32 v28, v24, v25 op_sel:[0,0,1]
	v_cvt_pk_fp8_f32 v29, v26, v27 op_sel:[0,0,1]
	v_pk_add_f32 v[20:21], v[178:179], v[4:5]
	v_pk_add_f32 v[22:23], v[186:187], v[8:9]
	v_mov_b32_e32 v30, v3
	v_mov_b32_e32 v31, v3
	v_pk_add_f32 v[24:25], v[180:181], v[6:7]
	v_pk_add_f32 v[26:27], v[188:189], v[10:11]
	v_cvt_pk_fp8_f32 v30, v20, v21
	v_cvt_pk_fp8_f32 v31, v22, v23
	v_cvt_pk_fp8_f32 v30, v24, v25 op_sel:[0,0,1]
	v_cvt_pk_fp8_f32 v31, v26, v27 op_sel:[0,0,1]
	s_waitcnt lgkmcnt(0)
	s_barrier
	ds_read_b128 v[48:51], v47 offset:12288
	ds_write_b64 v40, v[28:29]
	ds_write_b64 v41, v[30:31]
	s_waitcnt lgkmcnt(2)
	global_store_dwordx4 v45, v[48:51], s[40:41]
	s_add_u32 s40, s40, 0x4000
	s_addc_u32 s41, s41, 0
	v_pk_add_f32 v[20:21], v[108:109], v[12:13]
	v_pk_add_f32 v[22:23], v[116:117], v[16:17]
	v_mov_b32_e32 v56, v3
	v_mov_b32_e32 v57, v3
	v_pk_add_f32 v[24:25], v[110:111], v[14:15]
	v_pk_add_f32 v[26:27], v[118:119], v[18:19]
	v_cvt_pk_fp8_f32 v56, v20, v21
	v_cvt_pk_fp8_f32 v57, v22, v23
	v_cvt_pk_fp8_f32 v56, v24, v25 op_sel:[0,0,1]
	v_cvt_pk_fp8_f32 v57, v26, v27 op_sel:[0,0,1]
	v_pk_add_f32 v[20:21], v[190:191], v[4:5]
	v_pk_add_f32 v[22:23], v[194:195], v[8:9]
	v_mov_b32_e32 v58, v3
	v_mov_b32_e32 v59, v3
	v_pk_add_f32 v[24:25], v[192:193], v[6:7]
	v_pk_add_f32 v[26:27], v[196:197], v[10:11]
	v_cvt_pk_fp8_f32 v58, v20, v21
	v_cvt_pk_fp8_f32 v59, v22, v23
	v_cvt_pk_fp8_f32 v58, v24, v25 op_sel:[0,0,1]
	v_cvt_pk_fp8_f32 v59, v26, v27 op_sel:[0,0,1]
	s_waitcnt lgkmcnt(0)
	s_barrier
	ds_read_b128 v[32:35], v47
	ds_write_b64 v40, v[56:57] offset:12288
	ds_write_b64 v41, v[58:59] offset:12288
	s_waitcnt lgkmcnt(2)
	global_store_dwordx4 v45, v[32:35], s[40:41]
	s_add_u32 s40, s40, 0x4000
	s_addc_u32 s41, s41, 0
	s_waitcnt lgkmcnt(0)
	s_barrier
	ds_read_b128 v[48:51], v47 offset:12288
	s_waitcnt lgkmcnt(0)
	global_store_dwordx4 v45, v[48:51], s[40:41]
	s_cmp_eq_u32 s23, s66
	s_mov_b64 s[22:23], -1
	s_cbranch_scc1 .LBB0_979
	s_andn2_b64 vcc, exec, s[8:9]
	s_cbranch_vccnz .LBB0_999
	s_ashr_i32 s22, s20, 2
	s_ashr_i32 s23, s22, 31
	s_lshl_b64 s[22:23], s[22:23], 12
	s_add_u32 s3, s52, s22
	s_addc_u32 s21, s53, s23
	s_lshl_b32 s22, s20, 10
	s_and_b32 s22, s22, 0xc00
	s_add_u32 s22, s3, s22
	s_addc_u32 s23, s21, 0
	s_lshl_b32 s3, s68, 10
	s_and_b32 s3, s3, 0x400
	s_add_i32 s3, s3, 0
	s_add_i32 m0, s3, 0x24000
	s_nop 0
	global_load_lds_dwordx4 v223, s[22:23]
